# s3 + store-address arithmetic hoisted in gate/up and down epilogues (one 64-bit add per later store instead of a 7-instruction chain)
# speedup vs baseline: 1.0036x; 1.0036x over previous
.LBB0_1307:
	s_mov_b64 s[58:59], 0x10000
	s_mov_b64 s[60:61], 0x40000
	v_pk_mul_f32 v[8:9], v[154:155], s[2:3] op_sel_hi:[1,0]
	v_pk_mul_f32 v[12:13], v[146:147], s[2:3] op_sel_hi:[1,0]
	v_exp_f32_e32 v8, v8
	v_exp_f32_e32 v9, v9
	v_exp_f32_e32 v12, v12
	v_exp_f32_e32 v13, v13
	v_pk_mul_f32 v[16:17], v[138:139], s[2:3] op_sel_hi:[1,0]
	v_pk_mul_f32 v[20:21], v[130:131], s[2:3] op_sel_hi:[1,0]
	v_exp_f32_e32 v16, v16
	v_exp_f32_e32 v17, v17
	v_exp_f32_e32 v20, v20
	v_exp_f32_e32 v21, v21
	v_pk_fma_f32 v[8:9], v[8:9], s[82:83], s[82:83] op_sel_hi:[1,0,0]
	v_pk_fma_f32 v[12:13], v[12:13], s[82:83], s[82:83] op_sel_hi:[1,0,0]
	v_rcp_f32_e32 v8, v8
	v_rcp_f32_e32 v9, v9
	v_rcp_f32_e32 v12, v12
	v_rcp_f32_e32 v13, v13
	v_pk_fma_f32 v[16:17], v[16:17], s[82:83], s[82:83] op_sel_hi:[1,0,0]
	v_pk_fma_f32 v[20:21], v[20:21], s[82:83], s[82:83] op_sel_hi:[1,0,0]
	v_rcp_f32_e32 v16, v16
	v_rcp_f32_e32 v17, v17
	v_pk_mul_f32 v[2:3], v[154:155], v[158:159]
	v_rcp_f32_e32 v20, v20
	v_rcp_f32_e32 v21, v21
	v_pk_mul_f32 v[2:3], v[2:3], v[8:9]
	v_pk_mul_f32 v[8:9], v[156:157], s[2:3] op_sel_hi:[1,0]
	v_pk_mul_f32 v[10:11], v[146:147], v[150:151]
	v_exp_f32_e32 v8, v8
	v_exp_f32_e32 v9, v9
	v_pk_mul_f32 v[10:11], v[10:11], v[12:13]
	v_pk_mul_f32 v[12:13], v[148:149], s[2:3] op_sel_hi:[1,0]
	v_pk_mul_f32 v[14:15], v[138:139], v[142:143]
	v_exp_f32_e32 v12, v12
	v_exp_f32_e32 v13, v13
	v_pk_mul_f32 v[14:15], v[14:15], v[16:17]
	v_pk_mul_f32 v[16:17], v[140:141], s[2:3] op_sel_hi:[1,0]
	v_pk_mul_f32 v[18:19], v[130:131], v[134:135]
	v_exp_f32_e32 v16, v16
	v_exp_f32_e32 v17, v17
	v_pk_mul_f32 v[18:19], v[18:19], v[20:21]
	v_pk_mul_f32 v[20:21], v[132:133], s[2:3] op_sel_hi:[1,0]
	v_pk_fma_f32 v[8:9], v[8:9], s[82:83], s[82:83] op_sel_hi:[1,0,0]
	v_exp_f32_e32 v20, v20
	v_exp_f32_e32 v21, v21
	v_rcp_f32_e32 v8, v8
	v_rcp_f32_e32 v9, v9
	v_pk_fma_f32 v[12:13], v[12:13], s[82:83], s[82:83] op_sel_hi:[1,0,0]
	v_pk_fma_f32 v[16:17], v[16:17], s[82:83], s[82:83] op_sel_hi:[1,0,0]
	v_rcp_f32_e32 v12, v12
	v_rcp_f32_e32 v13, v13
	v_rcp_f32_e32 v16, v16
	v_rcp_f32_e32 v17, v17
	v_pk_fma_f32 v[20:21], v[20:21], s[82:83], s[82:83] op_sel_hi:[1,0,0]
	v_pk_mul_f32 v[6:7], v[156:157], v[160:161]
	v_rcp_f32_e32 v20, v20
	v_rcp_f32_e32 v21, v21
	v_pk_mul_f32 v[8:9], v[6:7], v[8:9]
	v_pk_mul_f32 v[6:7], v[148:149], v[152:153]
	v_lshl_add_u32 v4, s54, 8, v178
	v_pk_mul_f32 v[12:13], v[6:7], v[12:13]
	v_pk_mul_f32 v[6:7], v[140:141], v[144:145]
	s_lshl_b32 s24, s55, 7
	v_pk_mul_f32 v[16:17], v[6:7], v[16:17]
	v_pk_mul_f32 v[6:7], v[132:133], v[136:137]
	s_ashr_i32 s25, s24, 31
	v_pk_mul_f32 v[20:21], v[6:7], v[20:21]
	v_cvt_pk_fp8_f32 v6, v2, v3
	v_or_b32_e32 v2, v4, v179
	v_cvt_pk_fp8_f32 v7, v10, v11
	v_cvt_pk_fp8_f32 v6, v8, v9 op_sel:[0,0,1]
	v_cvt_pk_fp8_f32 v8, v14, v15
	v_cvt_pk_fp8_f32 v9, v18, v19
	v_ashrrev_i32_e32 v3, 31, v2
	v_lshlrev_b64 v[2:3], 11, v[2:3]
	v_lshl_add_u64 v[2:3], s[10:11], 0, v[2:3]
	v_lshl_add_u64 v[2:3], v[2:3], 0, s[24:25]
	v_cvt_pk_fp8_f32 v7, v12, v13 op_sel:[0,0,1]
	v_cvt_pk_fp8_f32 v8, v16, v17 op_sel:[0,0,1]
	v_cvt_pk_fp8_f32 v9, v20, v21 op_sel:[0,0,1]
	v_lshl_add_u64 v[2:3], v[2:3], 0, s[84:85]
	s_nop 1
	v_permlane16_swap_b32 v6, v8
	s_nop 1
	v_permlane16_swap_b32 v7, v9
	v_lshl_add_u64 v[250:251], v[2:3], 0, v[170:171]
	global_store_dwordx4 v[250:251], v[6:9], off nt
	v_pk_mul_f32 v[12:13], v[114:115], s[2:3] op_sel_hi:[1,0]
	v_pk_mul_f32 v[16:17], v[106:107], s[2:3] op_sel_hi:[1,0]
	v_pk_mul_f32 v[8:9], v[122:123], s[2:3] op_sel_hi:[1,0]
	v_exp_f32_e32 v12, v12
	v_exp_f32_e32 v8, v8
	v_exp_f32_e32 v9, v9
	v_exp_f32_e32 v13, v13
	v_exp_f32_e32 v16, v16
	v_exp_f32_e32 v17, v17
	v_pk_mul_f32 v[20:21], v[98:99], s[2:3] op_sel_hi:[1,0]
	v_pk_fma_f32 v[8:9], v[8:9], s[82:83], s[82:83] op_sel_hi:[1,0,0]
	v_exp_f32_e32 v20, v20
	v_exp_f32_e32 v21, v21
	v_rcp_f32_e32 v8, v8
	v_rcp_f32_e32 v9, v9
	v_pk_fma_f32 v[12:13], v[12:13], s[82:83], s[82:83] op_sel_hi:[1,0,0]
	v_pk_fma_f32 v[16:17], v[16:17], s[82:83], s[82:83] op_sel_hi:[1,0,0]
	v_rcp_f32_e32 v12, v12
	v_rcp_f32_e32 v13, v13
	v_rcp_f32_e32 v16, v16
	v_rcp_f32_e32 v17, v17
	v_pk_fma_f32 v[20:21], v[20:21], s[82:83], s[82:83] op_sel_hi:[1,0,0]
	v_pk_mul_f32 v[2:3], v[122:123], v[126:127]
	v_rcp_f32_e32 v20, v20
	v_rcp_f32_e32 v21, v21
	v_pk_mul_f32 v[2:3], v[2:3], v[8:9]
	v_pk_mul_f32 v[8:9], v[124:125], s[2:3] op_sel_hi:[1,0]
	v_pk_mul_f32 v[10:11], v[114:115], v[118:119]
	v_exp_f32_e32 v8, v8
	v_exp_f32_e32 v9, v9
	v_pk_mul_f32 v[10:11], v[10:11], v[12:13]
	v_pk_mul_f32 v[12:13], v[116:117], s[2:3] op_sel_hi:[1,0]
	v_pk_mul_f32 v[14:15], v[106:107], v[110:111]
	v_exp_f32_e32 v12, v12
	v_exp_f32_e32 v13, v13
	v_pk_mul_f32 v[14:15], v[14:15], v[16:17]
	v_pk_mul_f32 v[16:17], v[108:109], s[2:3] op_sel_hi:[1,0]
	v_pk_mul_f32 v[18:19], v[98:99], v[102:103]
	v_exp_f32_e32 v16, v16
	v_exp_f32_e32 v17, v17
	v_pk_mul_f32 v[18:19], v[18:19], v[20:21]
	v_pk_mul_f32 v[20:21], v[100:101], s[2:3] op_sel_hi:[1,0]
	v_pk_fma_f32 v[8:9], v[8:9], s[82:83], s[82:83] op_sel_hi:[1,0,0]
	v_exp_f32_e32 v20, v20
	v_exp_f32_e32 v21, v21
	v_rcp_f32_e32 v8, v8
	v_rcp_f32_e32 v9, v9
	v_pk_fma_f32 v[12:13], v[12:13], s[82:83], s[82:83] op_sel_hi:[1,0,0]
	v_pk_fma_f32 v[16:17], v[16:17], s[82:83], s[82:83] op_sel_hi:[1,0,0]
	v_rcp_f32_e32 v12, v12
	v_rcp_f32_e32 v13, v13
	v_rcp_f32_e32 v16, v16
	v_rcp_f32_e32 v17, v17
	v_pk_fma_f32 v[20:21], v[20:21], s[82:83], s[82:83] op_sel_hi:[1,0,0]
	v_pk_mul_f32 v[6:7], v[124:125], v[128:129]
	v_rcp_f32_e32 v20, v20
	v_rcp_f32_e32 v21, v21
	v_pk_mul_f32 v[8:9], v[6:7], v[8:9]
	v_pk_mul_f32 v[6:7], v[116:117], v[120:121]
	s_and_b64 vcc, exec, s[0:1]
	v_pk_mul_f32 v[12:13], v[6:7], v[12:13]
	v_pk_mul_f32 v[6:7], v[108:109], v[112:113]
	s_nop 0
	v_pk_mul_f32 v[16:17], v[6:7], v[16:17]
	v_pk_mul_f32 v[6:7], v[100:101], v[104:105]
	s_nop 0
	v_pk_mul_f32 v[20:21], v[6:7], v[20:21]
	v_cvt_pk_fp8_f32 v6, v2, v3
	v_cvt_pk_fp8_f32 v7, v10, v11
	v_cvt_pk_fp8_f32 v6, v8, v9 op_sel:[0,0,1]
	v_cvt_pk_fp8_f32 v8, v14, v15
	v_cvt_pk_fp8_f32 v9, v18, v19
	v_cvt_pk_fp8_f32 v7, v12, v13 op_sel:[0,0,1]
	v_cvt_pk_fp8_f32 v8, v16, v17 op_sel:[0,0,1]
	v_cvt_pk_fp8_f32 v9, v20, v21 op_sel:[0,0,1]
	s_nop 1
	v_permlane16_swap_b32 v6, v8
	s_nop 1
	v_permlane16_swap_b32 v7, v9
	v_lshl_add_u64 v[248:249], v[250:251], 0, s[58:59]
	global_store_dwordx4 v[248:249], v[6:9], off nt
	v_pk_mul_f32 v[12:13], v[82:83], s[2:3] op_sel_hi:[1,0]
	v_pk_mul_f32 v[16:17], v[74:75], s[2:3] op_sel_hi:[1,0]
	v_pk_mul_f32 v[8:9], v[90:91], s[2:3] op_sel_hi:[1,0]
	v_exp_f32_e32 v12, v12
	v_exp_f32_e32 v8, v8
	v_exp_f32_e32 v9, v9
	v_exp_f32_e32 v13, v13
	v_exp_f32_e32 v16, v16
	v_exp_f32_e32 v17, v17
	v_pk_mul_f32 v[20:21], v[66:67], s[2:3] op_sel_hi:[1,0]
	v_pk_fma_f32 v[8:9], v[8:9], s[82:83], s[82:83] op_sel_hi:[1,0,0]
	v_exp_f32_e32 v20, v20
	v_exp_f32_e32 v21, v21
	v_rcp_f32_e32 v8, v8
	v_rcp_f32_e32 v9, v9
	v_pk_fma_f32 v[12:13], v[12:13], s[82:83], s[82:83] op_sel_hi:[1,0,0]
	v_pk_fma_f32 v[16:17], v[16:17], s[82:83], s[82:83] op_sel_hi:[1,0,0]
	v_rcp_f32_e32 v12, v12
	v_rcp_f32_e32 v13, v13
	v_rcp_f32_e32 v16, v16
	v_rcp_f32_e32 v17, v17
	v_pk_fma_f32 v[20:21], v[20:21], s[82:83], s[82:83] op_sel_hi:[1,0,0]
	v_pk_mul_f32 v[2:3], v[90:91], v[94:95]
	v_rcp_f32_e32 v20, v20
	v_rcp_f32_e32 v21, v21
	v_pk_mul_f32 v[2:3], v[2:3], v[8:9]
	v_pk_mul_f32 v[8:9], v[92:93], s[2:3] op_sel_hi:[1,0]
	v_pk_mul_f32 v[10:11], v[82:83], v[86:87]
	v_exp_f32_e32 v8, v8
	v_exp_f32_e32 v9, v9
	v_pk_mul_f32 v[10:11], v[10:11], v[12:13]
	v_pk_mul_f32 v[12:13], v[84:85], s[2:3] op_sel_hi:[1,0]
	v_pk_mul_f32 v[14:15], v[74:75], v[78:79]
	v_exp_f32_e32 v12, v12
	v_exp_f32_e32 v13, v13
	v_pk_mul_f32 v[14:15], v[14:15], v[16:17]
	v_pk_mul_f32 v[16:17], v[76:77], s[2:3] op_sel_hi:[1,0]
	v_pk_mul_f32 v[18:19], v[66:67], v[70:71]
	v_exp_f32_e32 v16, v16
	v_exp_f32_e32 v17, v17
	v_pk_mul_f32 v[18:19], v[18:19], v[20:21]
	v_pk_mul_f32 v[20:21], v[68:69], s[2:3] op_sel_hi:[1,0]
	v_pk_fma_f32 v[8:9], v[8:9], s[82:83], s[82:83] op_sel_hi:[1,0,0]
	v_exp_f32_e32 v20, v20
	v_exp_f32_e32 v21, v21
	v_rcp_f32_e32 v8, v8
	v_rcp_f32_e32 v9, v9
	v_pk_fma_f32 v[12:13], v[12:13], s[82:83], s[82:83] op_sel_hi:[1,0,0]
	v_pk_fma_f32 v[16:17], v[16:17], s[82:83], s[82:83] op_sel_hi:[1,0,0]
	v_rcp_f32_e32 v12, v12
	v_rcp_f32_e32 v13, v13
	v_rcp_f32_e32 v16, v16
	v_rcp_f32_e32 v17, v17
	v_pk_fma_f32 v[20:21], v[20:21], s[82:83], s[82:83] op_sel_hi:[1,0,0]
	v_pk_mul_f32 v[6:7], v[92:93], v[96:97]
	v_rcp_f32_e32 v20, v20
	v_rcp_f32_e32 v21, v21
	v_pk_mul_f32 v[8:9], v[6:7], v[8:9]
	v_pk_mul_f32 v[6:7], v[84:85], v[88:89]
	v_pk_mul_f32 v[12:13], v[6:7], v[12:13]
	v_pk_mul_f32 v[6:7], v[76:77], v[80:81]
	s_nop 0
	v_pk_mul_f32 v[16:17], v[6:7], v[16:17]
	v_pk_mul_f32 v[6:7], v[68:69], v[72:73]
	s_nop 0
	v_pk_mul_f32 v[20:21], v[6:7], v[20:21]
	v_cvt_pk_fp8_f32 v6, v2, v3
	v_cvt_pk_fp8_f32 v7, v10, v11
	v_cvt_pk_fp8_f32 v6, v8, v9 op_sel:[0,0,1]
	v_cvt_pk_fp8_f32 v8, v14, v15
	v_cvt_pk_fp8_f32 v9, v18, v19
	v_cvt_pk_fp8_f32 v7, v12, v13 op_sel:[0,0,1]
	v_cvt_pk_fp8_f32 v8, v16, v17 op_sel:[0,0,1]
	v_cvt_pk_fp8_f32 v9, v20, v21 op_sel:[0,0,1]
	s_nop 1
	v_permlane16_swap_b32 v6, v8
	s_nop 1
	v_permlane16_swap_b32 v7, v9
	v_lshl_add_u64 v[246:247], v[250:251], 0, s[60:61]
	global_store_dwordx4 v[246:247], v[6:9], off nt
	v_pk_mul_f32 v[12:13], v[50:51], s[2:3] op_sel_hi:[1,0]
	v_pk_mul_f32 v[16:17], v[42:43], s[2:3] op_sel_hi:[1,0]
	v_pk_mul_f32 v[8:9], v[58:59], s[2:3] op_sel_hi:[1,0]
	v_exp_f32_e32 v12, v12
	v_exp_f32_e32 v8, v8
	v_exp_f32_e32 v9, v9
	v_exp_f32_e32 v13, v13
	v_exp_f32_e32 v16, v16
	v_exp_f32_e32 v17, v17
	v_pk_mul_f32 v[20:21], v[34:35], s[2:3] op_sel_hi:[1,0]
	v_pk_fma_f32 v[8:9], v[8:9], s[82:83], s[82:83] op_sel_hi:[1,0,0]
	v_exp_f32_e32 v20, v20
	v_exp_f32_e32 v21, v21
	v_rcp_f32_e32 v8, v8
	v_rcp_f32_e32 v9, v9
	v_pk_fma_f32 v[12:13], v[12:13], s[82:83], s[82:83] op_sel_hi:[1,0,0]
	v_pk_fma_f32 v[16:17], v[16:17], s[82:83], s[82:83] op_sel_hi:[1,0,0]
	v_rcp_f32_e32 v12, v12
	v_rcp_f32_e32 v13, v13
	v_rcp_f32_e32 v16, v16
	v_rcp_f32_e32 v17, v17
	v_pk_fma_f32 v[20:21], v[20:21], s[82:83], s[82:83] op_sel_hi:[1,0,0]
	v_pk_mul_f32 v[2:3], v[58:59], v[62:63]
	v_rcp_f32_e32 v20, v20
	v_rcp_f32_e32 v21, v21
	v_pk_mul_f32 v[2:3], v[2:3], v[8:9]
	v_pk_mul_f32 v[8:9], v[60:61], s[2:3] op_sel_hi:[1,0]
	v_pk_mul_f32 v[10:11], v[50:51], v[54:55]
	v_exp_f32_e32 v8, v8
	v_exp_f32_e32 v9, v9
	v_pk_mul_f32 v[10:11], v[10:11], v[12:13]
	v_pk_mul_f32 v[12:13], v[52:53], s[2:3] op_sel_hi:[1,0]
	v_pk_mul_f32 v[14:15], v[42:43], v[46:47]
	v_exp_f32_e32 v12, v12
	v_exp_f32_e32 v13, v13
	v_pk_mul_f32 v[14:15], v[14:15], v[16:17]
	v_pk_mul_f32 v[16:17], v[44:45], s[2:3] op_sel_hi:[1,0]
	v_pk_mul_f32 v[18:19], v[34:35], v[38:39]
	v_exp_f32_e32 v16, v16
	v_exp_f32_e32 v17, v17
	v_pk_mul_f32 v[18:19], v[18:19], v[20:21]
	v_pk_mul_f32 v[20:21], v[36:37], s[2:3] op_sel_hi:[1,0]
	v_pk_fma_f32 v[8:9], v[8:9], s[82:83], s[82:83] op_sel_hi:[1,0,0]
	v_exp_f32_e32 v20, v20
	v_exp_f32_e32 v21, v21
	v_rcp_f32_e32 v8, v8
	v_rcp_f32_e32 v9, v9
	v_pk_fma_f32 v[12:13], v[12:13], s[82:83], s[82:83] op_sel_hi:[1,0,0]
	v_pk_fma_f32 v[16:17], v[16:17], s[82:83], s[82:83] op_sel_hi:[1,0,0]
	v_rcp_f32_e32 v12, v12
	v_rcp_f32_e32 v13, v13
	v_rcp_f32_e32 v16, v16
	v_rcp_f32_e32 v17, v17
	v_pk_fma_f32 v[20:21], v[20:21], s[82:83], s[82:83] op_sel_hi:[1,0,0]
	v_pk_mul_f32 v[6:7], v[60:61], v[64:65]
	v_rcp_f32_e32 v20, v20
	v_rcp_f32_e32 v21, v21
	v_pk_mul_f32 v[8:9], v[6:7], v[8:9]
	v_pk_mul_f32 v[6:7], v[52:53], v[56:57]
	s_nop 0
	v_pk_mul_f32 v[12:13], v[6:7], v[12:13]
	v_pk_mul_f32 v[6:7], v[44:45], v[48:49]
	s_nop 0
	v_pk_mul_f32 v[16:17], v[6:7], v[16:17]
	v_pk_mul_f32 v[6:7], v[36:37], v[40:41]
	s_nop 0
	v_pk_mul_f32 v[20:21], v[6:7], v[20:21]
	v_cvt_pk_fp8_f32 v6, v2, v3
	v_cvt_pk_fp8_f32 v6, v8, v9 op_sel:[0,0,1]
	v_cvt_pk_fp8_f32 v7, v10, v11
	v_cvt_pk_fp8_f32 v8, v14, v15
	v_cvt_pk_fp8_f32 v9, v18, v19
	v_cvt_pk_fp8_f32 v7, v12, v13 op_sel:[0,0,1]
	v_cvt_pk_fp8_f32 v8, v16, v17 op_sel:[0,0,1]
	v_cvt_pk_fp8_f32 v9, v20, v21 op_sel:[0,0,1]
	v_lshl_add_u64 v[244:245], v[246:247], 0, s[58:59]
	s_mov_b64 s[24:25], -1
	s_nop 1
	v_permlane16_swap_b32 v6, v8
	s_nop 1
	v_permlane16_swap_b32 v7, v9
	global_store_dwordx4 v[244:245], v[6:9], off nt
	s_cbranch_vccnz .LBB0_1292
	s_andn2_b64 vcc, exec, s[8:9]
	s_cbranch_vccnz .LBB0_1291
	s_barrier
	s_branch .LBB0_1291

.LBB0_1377:
	s_mov_b64 s[20:21], 0x8000
	s_mov_b64 s[22:23], 0x18000
	v_lshl_add_u32 v12, s18, 8, v199
	v_or_b32_e32 v2, v12, v200
	v_ashrrev_i32_e32 v3, 31, v2
	v_lshlrev_b64 v[6:7], 10, v[2:3]
	v_pk_mul_f32 v[8:9], v[158:159], s[86:87] op_sel_hi:[1,0]
	v_cvt_pk_fp8_f32 v2, v8, v9
	v_pk_mul_f32 v[8:9], v[154:155], s[86:87] op_sel_hi:[1,0]
	v_cvt_pk_fp8_f32 v3, v8, v9
	v_pk_mul_f32 v[4:5], v[160:161], s[86:87] op_sel_hi:[1,0]
	v_pk_mul_f32 v[10:11], v[150:151], s[86:87] op_sel_hi:[1,0]
	v_cvt_pk_fp8_f32 v2, v4, v5 op_sel:[0,0,1]
	v_pk_mul_f32 v[4:5], v[156:157], s[86:87] op_sel_hi:[1,0]
	s_lshl_b32 s18, s19, 8
	v_cvt_pk_fp8_f32 v3, v4, v5 op_sel:[0,0,1]
	v_cvt_pk_fp8_f32 v4, v10, v11
	v_pk_mul_f32 v[10:11], v[146:147], s[86:87] op_sel_hi:[1,0]
	v_cvt_pk_fp8_f32 v5, v10, v11
	s_ashr_i32 s19, s18, 31
	v_lshl_add_u64 v[6:7], s[6:7], 0, v[6:7]
	v_pk_mul_f32 v[8:9], v[152:153], s[86:87] op_sel_hi:[1,0]
	v_lshl_add_u64 v[6:7], v[6:7], 0, s[18:19]
	v_cvt_pk_fp8_f32 v4, v8, v9 op_sel:[0,0,1]
	v_pk_mul_f32 v[8:9], v[148:149], s[86:87] op_sel_hi:[1,0]
	v_lshl_add_u64 v[6:7], v[6:7], 0, s[84:85]
	v_cvt_pk_fp8_f32 v5, v8, v9 op_sel:[0,0,1]
	s_nop 1
	v_permlane16_swap_b32 v2, v4
	v_lshl_add_u64 v[6:7], v[6:7], 0, v[166:167]
	s_nop 1
	v_permlane16_swap_b32 v3, v5
	global_store_dwordx4 v[6:7], v[2:5], off
	v_pk_mul_f32 v[8:9], v[142:143], s[86:87] op_sel_hi:[1,0]
	v_pk_mul_f32 v[10:11], v[134:135], s[86:87] op_sel_hi:[1,0]
	v_cvt_pk_fp8_f32 v2, v8, v9
	v_pk_mul_f32 v[8:9], v[138:139], s[86:87] op_sel_hi:[1,0]
	v_cvt_pk_fp8_f32 v3, v8, v9
	v_pk_mul_f32 v[4:5], v[144:145], s[86:87] op_sel_hi:[1,0]
	v_pk_mul_f32 v[8:9], v[136:137], s[86:87] op_sel_hi:[1,0]
	v_cvt_pk_fp8_f32 v2, v4, v5 op_sel:[0,0,1]
	v_pk_mul_f32 v[4:5], v[140:141], s[86:87] op_sel_hi:[1,0]
	s_and_b64 vcc, exec, s[0:1]
	v_cvt_pk_fp8_f32 v3, v4, v5 op_sel:[0,0,1]
	v_cvt_pk_fp8_f32 v4, v10, v11
	v_pk_mul_f32 v[10:11], v[130:131], s[86:87] op_sel_hi:[1,0]
	v_cvt_pk_fp8_f32 v5, v10, v11
	v_cvt_pk_fp8_f32 v4, v8, v9 op_sel:[0,0,1]
	v_pk_mul_f32 v[8:9], v[132:133], s[86:87] op_sel_hi:[1,0]
	s_nop 1
	v_permlane16_swap_b32 v2, v4
	v_pk_mul_f32 v[10:11], v[118:119], s[86:87] op_sel_hi:[1,0]
	v_cvt_pk_fp8_f32 v5, v8, v9 op_sel:[0,0,1]
	v_pk_mul_f32 v[8:9], v[126:127], s[86:87] op_sel_hi:[1,0]
	s_nop 1
	v_permlane16_swap_b32 v3, v5
	global_store_dwordx4 v[6:7], v[2:5], off offset:128
	s_nop 1
	v_cvt_pk_fp8_f32 v2, v8, v9
	v_pk_mul_f32 v[8:9], v[122:123], s[86:87] op_sel_hi:[1,0]
	v_cvt_pk_fp8_f32 v3, v8, v9
	v_pk_mul_f32 v[4:5], v[128:129], s[86:87] op_sel_hi:[1,0]
	v_cvt_pk_fp8_f32 v2, v4, v5 op_sel:[0,0,1]
	v_pk_mul_f32 v[4:5], v[124:125], s[86:87] op_sel_hi:[1,0]
	v_pk_mul_f32 v[8:9], v[120:121], s[86:87] op_sel_hi:[1,0]
	v_cvt_pk_fp8_f32 v3, v4, v5 op_sel:[0,0,1]
	v_cvt_pk_fp8_f32 v4, v10, v11
	v_pk_mul_f32 v[10:11], v[114:115], s[86:87] op_sel_hi:[1,0]
	v_cvt_pk_fp8_f32 v5, v10, v11
	v_cvt_pk_fp8_f32 v4, v8, v9 op_sel:[0,0,1]
	v_pk_mul_f32 v[8:9], v[116:117], s[86:87] op_sel_hi:[1,0]
	v_cvt_pk_fp8_f32 v5, v8, v9 op_sel:[0,0,1]
	s_nop 1
	v_permlane16_swap_b32 v2, v4
	v_lshl_add_u64 v[6:7], v[6:7], 0, s[20:21]
	s_nop 1
	v_permlane16_swap_b32 v3, v5
	global_store_dwordx4 v[6:7], v[2:5], off
	v_pk_mul_f32 v[8:9], v[110:111], s[86:87] op_sel_hi:[1,0]
	v_pk_mul_f32 v[10:11], v[98:99], s[86:87] op_sel_hi:[1,0]
	v_cvt_pk_fp8_f32 v2, v8, v9
	v_pk_mul_f32 v[8:9], v[106:107], s[86:87] op_sel_hi:[1,0]
	v_cvt_pk_fp8_f32 v3, v8, v9
	v_pk_mul_f32 v[4:5], v[112:113], s[86:87] op_sel_hi:[1,0]
	v_pk_mul_f32 v[8:9], v[100:101], s[86:87] op_sel_hi:[1,0]
	v_cvt_pk_fp8_f32 v2, v4, v5 op_sel:[0,0,1]
	v_pk_mul_f32 v[4:5], v[108:109], s[86:87] op_sel_hi:[1,0]
	v_cvt_pk_fp8_f32 v3, v4, v5 op_sel:[0,0,1]
	v_cvt_pk_fp8_f32 v4, v10, v11
	v_pk_mul_f32 v[10:11], v[90:91], s[86:87] op_sel_hi:[1,0]
	v_cvt_pk_fp8_f32 v5, v10, v11
	v_cvt_pk_fp8_f32 v4, v8, v9 op_sel:[0,0,1]
	v_pk_mul_f32 v[8:9], v[92:93], s[86:87] op_sel_hi:[1,0]
	s_nop 1
	v_permlane16_swap_b32 v2, v4
	v_pk_mul_f32 v[10:11], v[86:87], s[86:87] op_sel_hi:[1,0]
	v_cvt_pk_fp8_f32 v5, v8, v9 op_sel:[0,0,1]
	v_pk_mul_f32 v[8:9], v[102:103], s[86:87] op_sel_hi:[1,0]
	s_nop 1
	v_permlane16_swap_b32 v3, v5
	global_store_dwordx4 v[6:7], v[2:5], off offset:128
	s_nop 1
	v_cvt_pk_fp8_f32 v2, v8, v9
	v_pk_mul_f32 v[8:9], v[94:95], s[86:87] op_sel_hi:[1,0]
	v_cvt_pk_fp8_f32 v3, v8, v9
	v_pk_mul_f32 v[4:5], v[104:105], s[86:87] op_sel_hi:[1,0]
	v_cvt_pk_fp8_f32 v2, v4, v5 op_sel:[0,0,1]
	v_pk_mul_f32 v[4:5], v[96:97], s[86:87] op_sel_hi:[1,0]
	v_pk_mul_f32 v[8:9], v[88:89], s[86:87] op_sel_hi:[1,0]
	v_cvt_pk_fp8_f32 v3, v4, v5 op_sel:[0,0,1]
	v_cvt_pk_fp8_f32 v4, v10, v11
	v_pk_mul_f32 v[10:11], v[82:83], s[86:87] op_sel_hi:[1,0]
	v_cvt_pk_fp8_f32 v5, v10, v11
	v_cvt_pk_fp8_f32 v4, v8, v9 op_sel:[0,0,1]
	v_pk_mul_f32 v[8:9], v[84:85], s[86:87] op_sel_hi:[1,0]
	v_cvt_pk_fp8_f32 v5, v8, v9 op_sel:[0,0,1]
	s_nop 1
	v_permlane16_swap_b32 v2, v4
	v_lshl_add_u64 v[6:7], v[6:7], 0, s[22:23]
	s_nop 1
	v_permlane16_swap_b32 v3, v5
	global_store_dwordx4 v[6:7], v[2:5], off
	v_pk_mul_f32 v[8:9], v[78:79], s[86:87] op_sel_hi:[1,0]
	v_pk_mul_f32 v[10:11], v[70:71], s[86:87] op_sel_hi:[1,0]
	v_cvt_pk_fp8_f32 v2, v8, v9
	v_pk_mul_f32 v[8:9], v[74:75], s[86:87] op_sel_hi:[1,0]
	v_cvt_pk_fp8_f32 v3, v8, v9
	v_pk_mul_f32 v[4:5], v[80:81], s[86:87] op_sel_hi:[1,0]
	v_pk_mul_f32 v[8:9], v[72:73], s[86:87] op_sel_hi:[1,0]
	v_cvt_pk_fp8_f32 v2, v4, v5 op_sel:[0,0,1]
	v_pk_mul_f32 v[4:5], v[76:77], s[86:87] op_sel_hi:[1,0]
	s_nop 0
	v_cvt_pk_fp8_f32 v3, v4, v5 op_sel:[0,0,1]
	v_cvt_pk_fp8_f32 v4, v10, v11
	v_pk_mul_f32 v[10:11], v[66:67], s[86:87] op_sel_hi:[1,0]
	v_cvt_pk_fp8_f32 v5, v10, v11
	v_cvt_pk_fp8_f32 v4, v8, v9 op_sel:[0,0,1]
	v_pk_mul_f32 v[8:9], v[68:69], s[86:87] op_sel_hi:[1,0]
	s_nop 1
	v_permlane16_swap_b32 v2, v4
	v_pk_mul_f32 v[10:11], v[54:55], s[86:87] op_sel_hi:[1,0]
	v_cvt_pk_fp8_f32 v5, v8, v9 op_sel:[0,0,1]
	v_pk_mul_f32 v[8:9], v[62:63], s[86:87] op_sel_hi:[1,0]
	s_nop 1
	v_permlane16_swap_b32 v3, v5
	global_store_dwordx4 v[6:7], v[2:5], off offset:128
	s_nop 1
	v_cvt_pk_fp8_f32 v2, v8, v9
	v_pk_mul_f32 v[8:9], v[58:59], s[86:87] op_sel_hi:[1,0]
	v_cvt_pk_fp8_f32 v3, v8, v9
	v_pk_mul_f32 v[4:5], v[64:65], s[86:87] op_sel_hi:[1,0]
	v_cvt_pk_fp8_f32 v2, v4, v5 op_sel:[0,0,1]
	v_pk_mul_f32 v[4:5], v[60:61], s[86:87] op_sel_hi:[1,0]
	v_pk_mul_f32 v[8:9], v[56:57], s[86:87] op_sel_hi:[1,0]
	v_cvt_pk_fp8_f32 v3, v4, v5 op_sel:[0,0,1]
	v_cvt_pk_fp8_f32 v4, v10, v11
	v_pk_mul_f32 v[10:11], v[50:51], s[86:87] op_sel_hi:[1,0]
	v_cvt_pk_fp8_f32 v5, v10, v11
	v_cvt_pk_fp8_f32 v4, v8, v9 op_sel:[0,0,1]
	v_pk_mul_f32 v[8:9], v[52:53], s[86:87] op_sel_hi:[1,0]
	v_cvt_pk_fp8_f32 v5, v8, v9 op_sel:[0,0,1]
	s_nop 1
	v_permlane16_swap_b32 v2, v4
	v_lshl_add_u64 v[6:7], v[6:7], 0, s[20:21]
	s_nop 1
	v_permlane16_swap_b32 v3, v5
	global_store_dwordx4 v[6:7], v[2:5], off
	v_pk_mul_f32 v[8:9], v[46:47], s[86:87] op_sel_hi:[1,0]
	v_pk_mul_f32 v[10:11], v[38:39], s[86:87] op_sel_hi:[1,0]
	v_cvt_pk_fp8_f32 v2, v8, v9
	v_pk_mul_f32 v[8:9], v[42:43], s[86:87] op_sel_hi:[1,0]
	v_cvt_pk_fp8_f32 v3, v8, v9
	v_pk_mul_f32 v[4:5], v[48:49], s[86:87] op_sel_hi:[1,0]
	v_pk_mul_f32 v[8:9], v[40:41], s[86:87] op_sel_hi:[1,0]
	v_cvt_pk_fp8_f32 v2, v4, v5 op_sel:[0,0,1]
	v_pk_mul_f32 v[4:5], v[44:45], s[86:87] op_sel_hi:[1,0]
	s_mov_b64 s[18:19], -1
	v_cvt_pk_fp8_f32 v3, v4, v5 op_sel:[0,0,1]
	v_cvt_pk_fp8_f32 v4, v10, v11
	v_pk_mul_f32 v[10:11], v[34:35], s[86:87] op_sel_hi:[1,0]
	v_cvt_pk_fp8_f32 v5, v10, v11
	v_cvt_pk_fp8_f32 v4, v8, v9 op_sel:[0,0,1]
	v_pk_mul_f32 v[8:9], v[36:37], s[86:87] op_sel_hi:[1,0]
	s_nop 1
	v_permlane16_swap_b32 v2, v4
	s_nop 0
	v_cvt_pk_fp8_f32 v5, v8, v9 op_sel:[0,0,1]
	s_nop 0
	s_nop 1
	v_permlane16_swap_b32 v3, v5
	global_store_dwordx4 v[6:7], v[2:5], off offset:128
	s_cbranch_vccnz .LBB0_1364
	s_andn2_b64 vcc, exec, s[4:5]
	s_cbranch_vccnz .LBB0_1363
	s_barrier
	s_branch .LBB0_1363
